# WATT bias-table fill as one 4-load batch (was a 4-trip loop with a round trip each); MoE expert search reads the 16 tile prefixes in one LDS round trip
# baseline (speedup 1.0000x reference)
; template <int PH, bool PRB = false>
; __device__ __forceinline__ void run_phase(int layer, LAS unsigned char* lds, const int wv_) {
;     ...
;         for (int u = bid; u < (S / 64) * 2; u += G) {
;             const int kv = u & 1, blk = u >> 1;
;             for (int i = tid; i < 4 * 512; i += NT) { const int hq = i >> 9, d = (i & 511) - 256; tb[i] = (d >= -128 && d <= 128) ? bte[(kv * 4 + hq) * 257 + d + 128] * 1.4426950408889634f : -__builtin_inff(); }
.LBB0_645:
	s_and_b32 s18, s20, 1
	s_lshl_b32 s19, s18, 2
	s_and_saveexec_b64 s[0:1], s[4:5]
	s_cbranch_execz .LBB0_650
	v_mov_b32_e32 v4, 0xff800000
	v_mov_b32_e32 v5, 0xff800000
	v_mov_b32_e32 v6, 0xff800000
	v_mov_b32_e32 v7, 0xff800000
	s_and_saveexec_b64 s[10:11], s[6:7]
	s_cbranch_execz .Lwtab_skip
	v_ashrrev_i32_e32 v2, 9, v140
	v_add_u32_e32 v2, s19, v2
	v_mul_i32_i24_e32 v2, 0x101, v2
	v_ashrrev_i32_e32 v3, 31, v2
	v_lshl_add_u64 v[2:3], v[112:113], 0, v[2:3]
	v_lshl_add_u64 v[2:3], v[2:3], 2, s[2:3]
	v_add_co_u32_e32 v2, vcc, 0x213ffe00, v2
	s_nop 1
	v_addc_co_u32_e32 v3, vcc, 0, v3, vcc
	global_load_dword v4, v[2:3], off
	global_load_dword v5, v[2:3], off offset:1028
	global_load_dword v6, v[2:3], off offset:2056
	global_load_dword v7, v[2:3], off offset:3084
	s_waitcnt vmcnt(0)
	v_mul_f32_e32 v4, 0x3fb8aa3b, v4
	v_mul_f32_e32 v5, 0x3fb8aa3b, v5
	v_mul_f32_e32 v6, 0x3fb8aa3b, v6
	v_mul_f32_e32 v7, 0x3fb8aa3b, v7
.Lwtab_skip:
	s_or_b64 exec, exec, s[10:11]
	ds_write_b32 v141, v4
	ds_write_b32 v141, v5 offset:2048
	ds_write_b32 v141, v6 offset:4096
	ds_write_b32 v141, v7 offset:6144

;     __device__ __forceinline__ bool next(int i, Unit& u) const {
;         const int T = __builtin_amdgcn_readfirstlane(moe[16]), Ng = (T + 7) >> 3, x = c & 7, k = c >> 3; int g;
;         if (TOKEN_ROWS) g = x + 8 * i;
;         else { const int hc = Ng & 7, nl = 8 - hc;
;             if (x >= hc) g = i == 0 ? x - hc : nl + (i - 1) * 8 + (x - hc); else g = 2 * nl + 8 * i + x; }
;         if (g >= Ng) return false;
;         const int rt = g * 8 + (k >> 2); if (rt >= T) return false;
;         u.pn = k & 3; int e = 0;
; #pragma unroll
;         for (int j = 1; j < 16; ++j) e = (rt >= moe[j]) ? j : e;
;         e = __builtin_amdgcn_readfirstlane(e);
;         u.e = e; u.pm = __builtin_amdgcn_readfirstlane(rt - moe[e]); const int left = __builtin_amdgcn_readfirstlane(moe[17 + e]) - u.pm * BM; u.rows = left < BM ? left : BM; return true;
.LBB0_1587:
	s_or_b64 exec, exec, s[0:1]
	s_waitcnt lgkmcnt(0)
	s_barrier
	v_mbcnt_lo_u32_b32 v0, -1, 0
	v_mbcnt_hi_u32_b32 v0, -1, v0
	v_readlane_b32 s0, v254, 37
	v_add_u32_e32 v0, s93, v0
	s_and_b32 s42, s36, 7
	v_mov_b32_e32 v1, s0
	ds_read_b32 v1, v1
	v_readfirstlane_b32 s4, v0
	s_waitcnt lgkmcnt(0)
	v_readfirstlane_b32 s3, v1
	s_add_i32 s0, s3, 7
	s_ashr_i32 s0, s0, 3
	s_cmp_ge_i32 s42, s0
	s_mov_b64 s[0:1], 0
	s_cbranch_scc1 .LBB0_1590
	s_lshl_b32 s2, s42, 3
	s_ashr_i32 s0, s36, 5
	s_add_i32 s2, s2, s0
	s_cmp_ge_i32 s2, s3
	s_mov_b64 s[0:1], 0
	s_cbranch_scc1 .LBB0_1590
	v_readlane_b32 s0, v254, 29
	s_bfe_u32 s28, s36, 0x20003
	s_nop 0
	v_mov_b32_e32 v1, s0
	ds_read_b128 v[16:19], v1
	ds_read_b128 v[20:23], v1 offset:16
	ds_read_b128 v[24:27], v1 offset:32
	ds_read_b128 v[28:31], v1 offset:48
	s_mov_b32 s6, 0
	s_waitcnt lgkmcnt(0)
	v_readfirstlane_b32 s0, v17
	s_cmp_ge_i32 s2, s0
	s_addc_u32 s6, s6, 0
	v_readfirstlane_b32 s0, v18
	s_cmp_ge_i32 s2, s0
	s_addc_u32 s6, s6, 0
	v_readfirstlane_b32 s0, v19
	s_cmp_ge_i32 s2, s0
	s_addc_u32 s6, s6, 0
	v_readfirstlane_b32 s0, v20
	s_cmp_ge_i32 s2, s0
	s_addc_u32 s6, s6, 0
	v_readfirstlane_b32 s0, v21
	s_cmp_ge_i32 s2, s0
	s_addc_u32 s6, s6, 0
	v_readfirstlane_b32 s0, v22
	s_cmp_ge_i32 s2, s0
	s_addc_u32 s6, s6, 0
	v_readfirstlane_b32 s0, v23
	s_cmp_ge_i32 s2, s0
	s_addc_u32 s6, s6, 0
	v_readfirstlane_b32 s0, v24
	s_cmp_ge_i32 s2, s0
	s_addc_u32 s6, s6, 0
	v_readfirstlane_b32 s0, v25
	s_cmp_ge_i32 s2, s0
	s_addc_u32 s6, s6, 0
	v_readfirstlane_b32 s0, v26
	s_cmp_ge_i32 s2, s0
	s_addc_u32 s6, s6, 0
	v_readfirstlane_b32 s0, v27
	s_cmp_ge_i32 s2, s0
	s_addc_u32 s6, s6, 0
	v_readfirstlane_b32 s0, v28
	s_cmp_ge_i32 s2, s0
	s_addc_u32 s6, s6, 0
	v_readfirstlane_b32 s0, v29
	s_cmp_ge_i32 s2, s0
	s_addc_u32 s6, s6, 0
	v_readfirstlane_b32 s0, v30
	s_cmp_ge_i32 s2, s0
	s_addc_u32 s6, s6, 0
	v_readfirstlane_b32 s0, v31
	s_cmp_ge_i32 s2, s0
	s_addc_u32 s6, s6, 0
	s_lshl_b32 s0, s6, 2
	s_addk_i32 s0, 0x100
	s_add_i32 s0, s0, 0x20040
	v_mov_b32_e32 v1, s0
	ds_read2_b32 v[2:3], v1 offset1:17
	s_waitcnt lgkmcnt(0)
	v_sub_u32_e32 v1, s2, v2
	s_nop 0
	v_readfirstlane_b32 s33, v1
	v_readfirstlane_b32 s0, v3
	s_lshl_b32 s1, s33, 8
	s_sub_i32 s0, s0, s1
	s_min_i32 s40, s0, 0x100
	s_mov_b64 s[0:1], -1

;     __device__ __forceinline__ bool next(int i, Unit& u) const {
;         const int T = __builtin_amdgcn_readfirstlane(moe[16]), Ng = (T + 7) >> 3, x = c & 7, k = c >> 3; int g;
;         if (TOKEN_ROWS) g = x + 8 * i;
;         else { const int hc = Ng & 7, nl = 8 - hc;
;             if (x >= hc) g = i == 0 ? x - hc : nl + (i - 1) * 8 + (x - hc); else g = 2 * nl + 8 * i + x; }
;         if (g >= Ng) return false;
;         const int rt = g * 8 + (k >> 2); if (rt >= T) return false;
;         u.pn = k & 3; int e = 0;
; #pragma unroll
;         for (int j = 1; j < 16; ++j) e = (rt >= moe[j]) ? j : e;
;         e = __builtin_amdgcn_readfirstlane(e);
;         u.e = e; u.pm = __builtin_amdgcn_readfirstlane(rt - moe[e]); const int left = __builtin_amdgcn_readfirstlane(moe[17 + e]) - u.pm * BM; u.rows = left < BM ? left : BM; return true;
.LBB0_1596:
	v_readlane_b32 s4, v254, 37
	s_add_i32 s58, s58, 1
	s_mov_b64 s[30:31], 0
	v_mov_b32_e32 v0, s4
	ds_read_b32 v0, v0
	s_lshl_b32 s4, s58, 3
	s_or_b32 s4, s4, s42
	s_waitcnt lgkmcnt(0)
	v_readfirstlane_b32 s5, v0
	s_add_i32 s7, s5, 7
	s_ashr_i32 s7, s7, 3
	s_cmp_ge_i32 s4, s7
	s_cbranch_scc1 .LBB0_1599
	s_lshl_b32 s4, s4, 3
	s_add_i32 s4, s4, s57
	s_cmp_ge_i32 s4, s5
	s_cbranch_scc1 .LBB0_1599
	v_readlane_b32 s5, v254, 29
	s_mov_b64 s[30:31], -1
	s_nop 0
	v_mov_b32_e32 v0, s5
	ds_read_b128 v[16:19], v0
	ds_read_b128 v[20:23], v0 offset:16
	ds_read_b128 v[24:27], v0 offset:32
	ds_read_b128 v[28:31], v0 offset:48
	s_mov_b32 s24, 0
	s_waitcnt lgkmcnt(0)
	v_readfirstlane_b32 s5, v17
	s_cmp_ge_i32 s4, s5
	s_addc_u32 s24, s24, 0
	v_readfirstlane_b32 s5, v18
	s_cmp_ge_i32 s4, s5
	s_addc_u32 s24, s24, 0
	v_readfirstlane_b32 s5, v19
	s_cmp_ge_i32 s4, s5
	s_addc_u32 s24, s24, 0
	v_readfirstlane_b32 s5, v20
	s_cmp_ge_i32 s4, s5
	s_addc_u32 s24, s24, 0
	v_readfirstlane_b32 s5, v21
	s_cmp_ge_i32 s4, s5
	s_addc_u32 s24, s24, 0
	v_readfirstlane_b32 s5, v22
	s_cmp_ge_i32 s4, s5
	s_addc_u32 s24, s24, 0
	v_readfirstlane_b32 s5, v23
	s_cmp_ge_i32 s4, s5
	s_addc_u32 s24, s24, 0
	v_readfirstlane_b32 s5, v24
	s_cmp_ge_i32 s4, s5
	s_addc_u32 s24, s24, 0
	v_readfirstlane_b32 s5, v25
	s_cmp_ge_i32 s4, s5
	s_addc_u32 s24, s24, 0
	v_readfirstlane_b32 s5, v26
	s_cmp_ge_i32 s4, s5
	s_addc_u32 s24, s24, 0
	v_readfirstlane_b32 s5, v27
	s_cmp_ge_i32 s4, s5
	s_addc_u32 s24, s24, 0
	v_readfirstlane_b32 s5, v28
	s_cmp_ge_i32 s4, s5
	s_addc_u32 s24, s24, 0
	v_readfirstlane_b32 s5, v29
	s_cmp_ge_i32 s4, s5
	s_addc_u32 s24, s24, 0
	v_readfirstlane_b32 s5, v30
	s_cmp_ge_i32 s4, s5
	s_addc_u32 s24, s24, 0
	v_readfirstlane_b32 s5, v31
	s_cmp_ge_i32 s4, s5
	s_addc_u32 s24, s24, 0
	s_lshl_b32 s5, s24, 2
	s_addk_i32 s5, 0x100
	s_add_i32 s5, s5, 0x20040
	v_mov_b32_e32 v0, s5
	ds_read2_b32 v[0:1], v0 offset1:17
	s_waitcnt lgkmcnt(0)
	v_sub_u32_e32 v0, s4, v0
	s_nop 0
	v_readfirstlane_b32 s60, v0
	v_readfirstlane_b32 s4, v1
	s_lshl_b32 s5, s60, 8
	s_sub_i32 s4, s4, s5
	s_min_i32 s61, s4, 0x100

;     __device__ __forceinline__ bool next(int i, Unit& u) const {
;         const int T = __builtin_amdgcn_readfirstlane(moe[16]), Ng = (T + 7) >> 3, x = c & 7, k = c >> 3; int g;
;         if (TOKEN_ROWS) g = x + 8 * i;
;         else { const int hc = Ng & 7, nl = 8 - hc;
;             if (x >= hc) g = i == 0 ? x - hc : nl + (i - 1) * 8 + (x - hc); else g = 2 * nl + 8 * i + x; }
;         if (g >= Ng) return false;
;         const int rt = g * 8 + (k >> 2); if (rt >= T) return false;
;         u.pn = k & 3; int e = 0;
; #pragma unroll
;         for (int j = 1; j < 16; ++j) e = (rt >= moe[j]) ? j : e;
;         e = __builtin_amdgcn_readfirstlane(e);
;         u.e = e; u.pm = __builtin_amdgcn_readfirstlane(rt - moe[e]); const int left = __builtin_amdgcn_readfirstlane(moe[17 + e]) - u.pm * BM; u.rows = left < BM ? left : BM; return true;
.LBB0_1628:
	v_mbcnt_lo_u32_b32 v0, -1, 0
	v_mbcnt_hi_u32_b32 v0, -1, v0
	v_readlane_b32 s0, v254, 37
	v_add_u32_e32 v2, s93, v0
	s_or_b32 s33, s42, 16
	v_mov_b32_e32 v0, s0
	ds_read_b32 v0, v0
	v_readfirstlane_b32 s16, v2
	s_waitcnt lgkmcnt(0)
	v_readfirstlane_b32 s4, v0
	s_add_i32 s0, s4, 7
	s_ashr_i32 s2, s0, 3
	s_and_b32 s0, s2, 7
	v_mov_b32_e32 v0, s0
	s_lshl_b32 s0, s0, 1
	v_sub_co_u32_e32 v0, vcc, s42, v0
	s_sub_i32 s3, s33, s0
	s_and_b64 s[0:1], vcc, exec
	v_readfirstlane_b32 s0, v0
	s_cselect_b32 s1, s3, s0
	s_cmp_ge_i32 s1, s2
	s_mov_b64 s[2:3], 0
	s_cbranch_scc1 .LBB0_1631
	s_lshl_b32 s1, s1, 3
	s_ashr_i32 s0, s36, 5
	s_add_i32 s1, s1, s0
	s_cmp_ge_i32 s1, s4
	s_cbranch_scc1 .LBB0_1631
	v_readlane_b32 s2, v254, 29
	s_bfe_u32 s0, s36, 0x20003
	s_nop 0
	v_mov_b32_e32 v0, s2
	ds_read_b128 v[16:19], v0
	ds_read_b128 v[20:23], v0 offset:16
	ds_read_b128 v[24:27], v0 offset:32
	ds_read_b128 v[28:31], v0 offset:48
	s_mov_b32 s20, 0
	s_waitcnt lgkmcnt(0)
	v_readfirstlane_b32 s2, v17
	s_cmp_ge_i32 s1, s2
	s_addc_u32 s20, s20, 0
	v_readfirstlane_b32 s2, v18
	s_cmp_ge_i32 s1, s2
	s_addc_u32 s20, s20, 0
	v_readfirstlane_b32 s2, v19
	s_cmp_ge_i32 s1, s2
	s_addc_u32 s20, s20, 0
	v_readfirstlane_b32 s2, v20
	s_cmp_ge_i32 s1, s2
	s_addc_u32 s20, s20, 0
	v_readfirstlane_b32 s2, v21
	s_cmp_ge_i32 s1, s2
	s_addc_u32 s20, s20, 0
	v_readfirstlane_b32 s2, v22
	s_cmp_ge_i32 s1, s2
	s_addc_u32 s20, s20, 0
	v_readfirstlane_b32 s2, v23
	s_cmp_ge_i32 s1, s2
	s_addc_u32 s20, s20, 0
	v_readfirstlane_b32 s2, v24
	s_cmp_ge_i32 s1, s2
	s_addc_u32 s20, s20, 0
	v_readfirstlane_b32 s2, v25
	s_cmp_ge_i32 s1, s2
	s_addc_u32 s20, s20, 0
	v_readfirstlane_b32 s2, v26
	s_cmp_ge_i32 s1, s2
	s_addc_u32 s20, s20, 0
	v_readfirstlane_b32 s2, v27
	s_cmp_ge_i32 s1, s2
	s_addc_u32 s20, s20, 0
	v_readfirstlane_b32 s2, v28
	s_cmp_ge_i32 s1, s2
	s_addc_u32 s20, s20, 0
	v_readfirstlane_b32 s2, v29
	s_cmp_ge_i32 s1, s2
	s_addc_u32 s20, s20, 0
	v_readfirstlane_b32 s2, v30
	s_cmp_ge_i32 s1, s2
	s_addc_u32 s20, s20, 0
	v_readfirstlane_b32 s2, v31
	s_cmp_ge_i32 s1, s2
	s_addc_u32 s20, s20, 0
	s_lshl_b32 s2, s20, 2
	s_addk_i32 s2, 0x100
	s_add_i32 s2, s2, 0x20040
	v_mov_b32_e32 v0, s2
	ds_read2_b32 v[0:1], v0 offset1:17
	s_waitcnt lgkmcnt(0)
	v_sub_u32_e32 v0, s1, v0
	s_nop 0
	v_readfirstlane_b32 s63, v0
	v_readfirstlane_b32 s1, v1
	s_lshl_b32 s2, s63, 8
	s_sub_i32 s1, s1, s2
	s_min_i32 s38, s1, 0x100
	s_mov_b64 s[2:3], -1

;     __device__ __forceinline__ bool next(int i, Unit& u) const {
;         const int T = __builtin_amdgcn_readfirstlane(moe[16]), Ng = (T + 7) >> 3, x = c & 7, k = c >> 3; int g;
;         if (TOKEN_ROWS) g = x + 8 * i;
;         else { const int hc = Ng & 7, nl = 8 - hc;
;             if (x >= hc) g = i == 0 ? x - hc : nl + (i - 1) * 8 + (x - hc); else g = 2 * nl + 8 * i + x; }
;         if (g >= Ng) return false;
;         const int rt = g * 8 + (k >> 2); if (rt >= T) return false;
;         u.pn = k & 3; int e = 0;
; #pragma unroll
;         for (int j = 1; j < 16; ++j) e = (rt >= moe[j]) ? j : e;
;         e = __builtin_amdgcn_readfirstlane(e);
;         u.e = e; u.pm = __builtin_amdgcn_readfirstlane(rt - moe[e]); const int left = __builtin_amdgcn_readfirstlane(moe[17 + e]) - u.pm * BM; u.rows = left < BM ? left : BM; return true;
.LBB0_1652:
	v_readlane_b32 s1, v254, 37
	s_add_i32 s62, s62, 1
	s_mov_b64 s[28:29], 0
	v_mov_b32_e32 v0, s1
	ds_read_b32 v0, v0
	s_lshl_b32 s1, s62, 3
	s_add_i32 s5, s1, s33
	s_or_b32 s1, s1, s42
	s_waitcnt lgkmcnt(0)
	v_readfirstlane_b32 s4, v0
	s_add_i32 s6, s4, 7
	s_ashr_i32 s6, s6, 3
	s_and_b32 s7, s6, 7
	s_lshl_b32 s19, s7, 1
	s_cmp_lt_u32 s42, s7
	s_cselect_b32 s1, s5, s1
	s_sub_i32 s1, s1, s19
	s_cmp_ge_i32 s1, s6
	s_cbranch_scc1 .LBB0_1655
	s_lshl_b32 s1, s1, 3
	s_add_i32 s1, s1, s61
	s_mov_b32 s101, s1
	s_cmp_ge_i32 s1, s4
	s_cbranch_scc1 .LBB0_1655
	v_readlane_b32 s4, v254, 29
	s_mov_b64 s[28:29], -1
	s_nop 0
	v_mov_b32_e32 v0, s4
	ds_read_b128 v[16:19], v0
	ds_read_b128 v[20:23], v0 offset:16
	ds_read_b128 v[24:27], v0 offset:32
	ds_read_b128 v[28:31], v0 offset:48
	s_mov_b32 s22, 0
	s_waitcnt lgkmcnt(0)
	v_readfirstlane_b32 s4, v17
	s_cmp_ge_i32 s1, s4
	s_addc_u32 s22, s22, 0
	v_readfirstlane_b32 s4, v18
	s_cmp_ge_i32 s1, s4
	s_addc_u32 s22, s22, 0
	v_readfirstlane_b32 s4, v19
	s_cmp_ge_i32 s1, s4
	s_addc_u32 s22, s22, 0
	v_readfirstlane_b32 s4, v20
	s_cmp_ge_i32 s1, s4
	s_addc_u32 s22, s22, 0
	v_readfirstlane_b32 s4, v21
	s_cmp_ge_i32 s1, s4
	s_addc_u32 s22, s22, 0
	v_readfirstlane_b32 s4, v22
	s_cmp_ge_i32 s1, s4
	s_addc_u32 s22, s22, 0
	v_readfirstlane_b32 s4, v23
	s_cmp_ge_i32 s1, s4
	s_addc_u32 s22, s22, 0
	v_readfirstlane_b32 s4, v24
	s_cmp_ge_i32 s1, s4
	s_addc_u32 s22, s22, 0
	v_readfirstlane_b32 s4, v25
	s_cmp_ge_i32 s1, s4
	s_addc_u32 s22, s22, 0
	v_readfirstlane_b32 s4, v26
	s_cmp_ge_i32 s1, s4
	s_addc_u32 s22, s22, 0
	v_readfirstlane_b32 s4, v27
	s_cmp_ge_i32 s1, s4
	s_addc_u32 s22, s22, 0
	v_readfirstlane_b32 s4, v28
	s_cmp_ge_i32 s1, s4
	s_addc_u32 s22, s22, 0
	v_readfirstlane_b32 s4, v29
	s_cmp_ge_i32 s1, s4
	s_addc_u32 s22, s22, 0
	v_readfirstlane_b32 s4, v30
	s_cmp_ge_i32 s1, s4
	s_addc_u32 s22, s22, 0
	v_readfirstlane_b32 s4, v31
	s_cmp_ge_i32 s1, s4
	s_addc_u32 s22, s22, 0
	s_lshl_b32 s4, s22, 2
	s_addk_i32 s4, 0x100
	s_add_i32 s4, s4, 0x20040
	v_mov_b32_e32 v0, s4
	ds_read2_b32 v[0:1], v0 offset1:17
	s_waitcnt lgkmcnt(0)
	v_sub_u32_e32 v0, s1, v0
	s_nop 0
	v_readfirstlane_b32 s64, v0
	v_readfirstlane_b32 s1, v1
	s_lshl_b32 s4, s64, 8
	s_sub_i32 s1, s1, s4
	s_min_i32 s65, s1, 0x100
